# MoE tile-to-expert lookup: replaced the unrolled 31-entry LDS scan with an incremental monotone search in both expert GEMM phases
# speedup vs baseline: 1.0128x; 1.0038x over previous
;     __device__ bool next(int i, Unit& u) const {
;         const int L = i * G + c, TT = tb[NE]; if (L >= TT * nPN) return false;
;         const int t = L / nPN; u.pm = t; u.pn = L - t * nPN; int e = 0;
;         for (int j = 1; j < NE; ++j) e += (tb[j] <= t) ? 1 : 0;
;         u.ex = e; return true;
;     }
.LBB0_2141:
	ds_read_b32 v2, v208
	s_add_i32 s38, s38, 1
	s_mul_i32 s0, s38, s93
	s_add_i32 s0, s0, s84
	s_waitcnt lgkmcnt(0)
	v_readfirstlane_b32 s1, v2
	s_lshl_b32 s1, s1, 4
	s_cmp_lt_i32 s0, s1
	s_cselect_b64 s[30:31], -1, 0
	s_cmp_ge_i32 s0, s1
	s_cbranch_scc1 .LBB0_2143
	s_ashr_i32 s1, s0, 31
	s_lshr_b32 s1, s1, 28
	s_add_i32 s1, s0, s1
	s_ashr_i32 s75, s1, 4
	s_and_b32 s1, s1, -16
	s_sub_i32 s26, s0, s1
	v_readfirstlane_b32 s1, v170
.Lm1_srch:
	s_cmp_gt_i32 s1, 30
	s_cbranch_scc1 .Lm1_done
	s_lshl_b32 s98, s1, 2
	s_add_i32 s98, s98, 0x20404
	v_mov_b32_e32 v2, s98
	ds_read_b32 v2, v2
	s_waitcnt lgkmcnt(0)
	v_readfirstlane_b32 s99, v2
	s_cmp_le_i32 s99, s75
	s_cbranch_scc0 .Lm1_done
	s_add_i32 s1, s1, 1
	s_branch .Lm1_srch
.Lm1_done:
	v_mov_b32_e32 v166, s1

;     __device__ bool next(int i, Unit& u) const {
;         const int L = i * G + c, TT = tb[NE]; if (L >= TT * nPN) return false;
;         const int t = L / nPN; u.pm = t; u.pn = L - t * nPN; int e = 0;
;         for (int j = 1; j < NE; ++j) e += (tb[j] <= t) ? 1 : 0;
;         u.ex = e; return true;
;     }
.LBB0_2220:
	ds_read_b32 v2, v201
	s_add_i32 s41, s41, 1
	s_mul_i32 s0, s41, s93
	s_add_i32 s0, s0, s84
	s_waitcnt lgkmcnt(0)
	v_readfirstlane_b32 s1, v2
	s_lshl_b32 s1, s1, 3
	s_cmp_lt_i32 s0, s1
	s_cselect_b64 s[28:29], -1, 0
	s_cmp_ge_i32 s0, s1
	s_cbranch_scc1 .LBB0_2222
	s_ashr_i32 s1, s0, 31
	s_lshr_b32 s1, s1, 29
	s_add_i32 s1, s0, s1
	s_ashr_i32 s20, s1, 3
	s_and_b32 s1, s1, -8
	s_sub_i32 s22, s0, s1
	v_readfirstlane_b32 s1, v178
.Lm2_srch:
	s_cmp_gt_i32 s1, 30
	s_cbranch_scc1 .Lm2_done
	s_lshl_b32 s98, s1, 2
	s_add_i32 s98, s98, 0x20404
	v_mov_b32_e32 v2, s98
	ds_read_b32 v2, v2
	s_waitcnt lgkmcnt(0)
	v_readfirstlane_b32 s99, v2
	s_cmp_le_i32 s99, s20
	s_cbranch_scc0 .Lm2_done
	s_add_i32 s1, s1, 1
	s_branch .Lm2_srch
.Lm2_done:
	v_mov_b32_e32 v176, s1

; #define LAS __attribute__((address_space(3)))
; __global__ void __launch_bounds__(NTHR, 2) mega(Args args) {
;     extern __shared__ __attribute__((aligned(16))) unsigned char lds_raw[];
;     Frame F;
;     F.lds = (LAS unsigned char*)lds_raw;
;     F.MISC = (volatile LAS unsigned*)(F.lds + MISC_OFF);
;     F.wave = __builtin_amdgcn_readfirstlane(threadIdx.x >> 6);
	.amdhsa_kernel _ZN2mk4megaENS_4ArgsE
		.amdhsa_group_segment_fixed_size 0
		.amdhsa_private_segment_fixed_size 0
		.amdhsa_kernarg_size 448
		.amdhsa_user_sgpr_count 2
		.amdhsa_user_sgpr_dispatch_ptr 0
		.amdhsa_user_sgpr_queue_ptr 0
		.amdhsa_user_sgpr_kernarg_segment_ptr 1
		.amdhsa_user_sgpr_dispatch_id 0
		.amdhsa_user_sgpr_kernarg_preload_length 0
		.amdhsa_user_sgpr_kernarg_preload_offset 0
		.amdhsa_user_sgpr_private_segment_size 0
		.amdhsa_uses_dynamic_stack 0
		.amdhsa_enable_private_segment 0
		.amdhsa_system_sgpr_workgroup_id_x 1
		.amdhsa_system_sgpr_workgroup_id_y 0
		.amdhsa_system_sgpr_workgroup_id_z 0
		.amdhsa_system_sgpr_workgroup_info 0
		.amdhsa_system_vgpr_workitem_id 0
		.amdhsa_next_free_vgpr 256
		.amdhsa_next_free_sgpr 102
		.amdhsa_accum_offset 256
		.amdhsa_reserve_vcc 1
		.amdhsa_float_round_mode_32 0
		.amdhsa_float_round_mode_16_64 0
		.amdhsa_float_denorm_mode_32 3
		.amdhsa_float_denorm_mode_16_64 3
		.amdhsa_dx10_clamp 1
		.amdhsa_ieee_mode 1
		.amdhsa_fp16_overflow 0
		.amdhsa_tg_split 0
		.amdhsa_exception_fp_ieee_invalid_op 0
		.amdhsa_exception_fp_denorm_src 0
		.amdhsa_exception_fp_ieee_div_zero 0
		.amdhsa_exception_fp_ieee_overflow 0
		.amdhsa_exception_fp_ieee_underflow 0
		.amdhsa_exception_fp_ieee_inexact 0
		.amdhsa_exception_int_div_zero 0
	.end_amdhsa_kernel

; __global__ void __launch_bounds__(NTHR, 2) mega(Args args) {
;     extern __shared__ __attribute__((aligned(16))) unsigned char lds_raw[];
amdhsa.kernels:
  - .agpr_count:     0
    .args:
      - .offset:         0
        .size:           192
        .value_kind:     by_value
      - .offset:         192
        .size:           4
        .value_kind:     hidden_block_count_x
      - .offset:         196
        .size:           4
        .value_kind:     hidden_block_count_y
      - .offset:         200
        .size:           4
        .value_kind:     hidden_block_count_z
      - .offset:         204
        .size:           2
        .value_kind:     hidden_group_size_x
      - .offset:         206
        .size:           2
        .value_kind:     hidden_group_size_y
      - .offset:         208
        .size:           2
        .value_kind:     hidden_group_size_z
      - .offset:         210
        .size:           2
        .value_kind:     hidden_remainder_x
      - .offset:         212
        .size:           2
        .value_kind:     hidden_remainder_y
      - .offset:         214
        .size:           2
        .value_kind:     hidden_remainder_z
      - .offset:         232
        .size:           8
        .value_kind:     hidden_global_offset_x
      - .offset:         240
        .size:           8
        .value_kind:     hidden_global_offset_y
      - .offset:         248
        .size:           8
        .value_kind:     hidden_global_offset_z
      - .offset:         256
        .size:           2
        .value_kind:     hidden_grid_dims
      - .offset:         312
        .size:           4
        .value_kind:     hidden_dynamic_lds_size
    .group_segment_fixed_size: 0
    .kernarg_segment_align: 8
    .kernarg_segment_size: 448
    .language:       OpenCL C
    .language_version:
      - 2
      - 0
    .max_flat_workgroup_size: 512
    .name:           _ZN2mk4megaENS_4ArgsE
    .private_segment_fixed_size: 0
    .sgpr_count:     108
    .sgpr_spill_count: 141
    .symbol:         _ZN2mk4megaENS_4ArgsE.kd
    .uniform_work_group_size: 1
    .uses_dynamic_stack: false
    .vgpr_count:     256
    .vgpr_spill_count: 0
    .wavefront_size: 64
